# rwkv_out: operand fragment loads (G^T / state) requested before the Yloc tile's LDS writes instead of after
# baseline (speedup 1.0000x reference)
; #define LAS __attribute__((address_space(3)))
; __device__ __forceinline__ int lt_tid(int wv) { int ln; asm volatile("v_mbcnt_lo_u32_b32 %0, -1, 0\n\tv_mbcnt_hi_u32_b32 %0, -1, %0" : "=v"(ln)); return (wv << 6) | ln; }
; __device__ __forceinline__ void ph_rwkv_out(const Params& p, int l, LAS unsigned char* lds, const int wvid) {
;     ...
;         const int lane = lt_tid(wvid) & 63, l31 = lane & 31, hi = lane >> 5;
;         const int bh = unit / RCH, ch = unit % RCH, b = bh >> 2, h = bh & 3, t0 = ch * 64;
;         const size_t uo = (size_t)unit * 4096;
;         const bf16_t* GTg = (const bf16_t*)(ws + WS_RWB + RW_GT) + uo; const bf16_t* YLg = (const bf16_t*)(ws + WS_RWB + RW_YL) + uo; const bf16_t* VVg = (const bf16_t*)(ob + RO_VV) + uo;
;         const u32x4* SH = (const u32x4*)(ob + RO_SH) + (size_t)unit * 512;
;         LAS unsigned char* X = lds + wave * (2 * R2_MB); LAS unsigned char* Y = X + R2_MB;
;         R2_RAW(X, VVg); R2_RAW(Y, YLg);
;         bf16x8 ga[4][2], sb[4][2]; unsigned short yl[2][2][16];
; #pragma unroll
;         for (int ks = 0; ks < 4; ++ks)
; #pragma unroll
;             for (int x = 0; x < 2; ++x) { ga[ks][x] = *(const bf16x8*)(GTg + TM(32 * x + l31, 16 * ks + 8 * hi)); sb[ks][x] = __builtin_bit_cast(bf16x8, SH[(x * 4 + ks) * 64 + lane]); }
.LBB0_856:
	s_mul_hi_i32 s1, s0, 0x7e07e07f
	s_lshr_b32 s6, s1, 31
	s_ashr_i32 s1, s1, 5
	s_add_i32 s8, s1, s6
	s_mul_i32 s1, s8, 0x41
	s_sub_i32 s16, s0, s1
	s_ashr_i32 s1, s0, 31
	s_and_b32 s9, s8, 3
	s_lshl_b64 s[0:1], s[0:1], 13
	s_add_u32 s6, s20, s0
	v_mbcnt_lo_u32_b32 v0, -1, 0
	v_mbcnt_hi_u32_b32 v0, -1, v0
	s_addc_u32 s7, s21, s1
	v_and_b32_e32 v34, 63, v0
	s_add_u32 s10, s30, s0
	s_waitcnt lgkmcnt(11)
	v_lshlrev_b32_e32 v90, 4, v34
	s_addc_u32 s11, s31, s1
	s_waitcnt lgkmcnt(2)
	v_or_b32_e32 v35, 0x1000, v90
	v_or_b32_e32 v37, 0x1800, v90
	global_load_dwordx4 v[2:5], v90, s[10:11]
	global_load_dwordx4 v[6:9], v90, s[10:11] offset:1024
	global_load_dwordx4 v[10:13], v90, s[10:11] offset:2048
	global_load_dwordx4 v[14:17], v90, s[10:11] offset:3072
	v_or_b32_e32 v36, 0x1400, v90
	global_load_dwordx4 v[18:21], v35, s[10:11]
	global_load_dwordx4 v[22:25], v36, s[10:11]
	v_or_b32_e32 v38, 0x1c00, v90
	global_load_dwordx4 v[26:29], v37, s[10:11]
	global_load_dwordx4 v[30:33], v38, s[10:11]
	v_lshlrev_b32_e32 v39, 4, v0
	v_bfe_u32 v40, v0, 1, 5
	v_or_b32_e32 v34, 64, v34
	v_and_b32_e32 v39, 16, v39
	v_mul_u32_u24_e32 v40, 0x90, v40
	v_lshrrev_b32_e32 v34, 1, v34
	v_add3_u32 v40, s34, v40, v39
	v_mul_u32_u24_e32 v34, 0x90, v34
	s_ashr_i32 s8, s8, 2
	v_add3_u32 v39, s34, v34, v39
	s_add_u32 s10, s28, s0
	s_addc_u32 s11, s29, s1
	s_waitcnt vmcnt(33)
	v_bfe_u32 v103, v0, 5, 1
	s_waitcnt vmcnt(28)
	v_lshlrev_b32_e32 v96, 2, v103
	s_lshl_b32 s35, s16, 6
	v_or_b32_e32 v110, 32, v96
	v_mov_b32_e32 v34, 0x5a0
	s_add_u32 s0, s2, s0
	s_waitcnt vmcnt(24)
	global_load_dwordx4 v[200:203], v90, s[10:11]
	global_load_dwordx4 v[206:209], v90, s[10:11] offset:1024
	global_load_dwordx4 v[210:213], v90, s[10:11] offset:2048
	global_load_dwordx4 v[232:235], v90, s[10:11] offset:3072
	global_load_dwordx4 v[236:239], v35, s[10:11]
	global_load_dwordx4 v[240:243], v36, s[10:11]
	global_load_dwordx4 v[244:247], v37, s[10:11]
	global_load_dwordx4 v[196:199], v38, s[10:11]
	v_mov_b32_e32 v91, v1
	v_and_b32_e32 v100, 31, v0
	s_addc_u32 s1, s3, s1
	v_lshlrev_b32_e32 v0, 5, v100
	v_lshl_or_b32 v0, v103, 4, v0
	v_lshl_add_u64 v[94:95], s[6:7], 0, v[0:1]
	v_or_b32_e32 v98, 1, v96
	v_readlane_b32 s48, v253, 46
	v_readlane_b32 s49, v253, 47
	v_readlane_b32 s50, v253, 48
	v_readlane_b32 s51, v253, 49
	v_readlane_b32 s52, v253, 50
	v_readlane_b32 s53, v253, 51
	v_readlane_b32 s54, v253, 52
	v_readlane_b32 s55, v253, 53
	v_readlane_b32 s56, v253, 54
	v_readlane_b32 s57, v253, 55
	v_readlane_b32 s58, v253, 56
	v_readlane_b32 s59, v253, 57
	v_readlane_b32 s60, v253, 58
	v_readlane_b32 s61, v253, 59
	v_readlane_b32 s62, v253, 60
	v_readlane_b32 s63, v253, 61
	s_mov_b64 s[48:49], s[52:53]
	s_mov_b64 s[50:51], s[54:55]
	s_mov_b64 s[52:53], s[56:57]
	s_mov_b64 s[54:55], s[58:59]
	s_mov_b64 s[56:57], s[60:61]
	s_movk_i32 s70, 0x1000
	s_mov_b64 s[58:59], s[62:63]
	s_waitcnt vmcnt(15)
	ds_write_b128 v40, v[2:5]
	s_waitcnt vmcnt(14)
	ds_write_b128 v39, v[6:9]
	s_waitcnt vmcnt(13)
	ds_write_b128 v40, v[10:13] offset:32
	s_waitcnt vmcnt(12)
	ds_write_b128 v39, v[14:17] offset:32
	s_waitcnt vmcnt(11)
	ds_write_b128 v40, v[18:21] offset:64
	s_waitcnt vmcnt(10)
	ds_write_b128 v40, v[22:25] offset:4672
	s_waitcnt vmcnt(9)
	ds_write_b128 v40, v[26:29] offset:96
	s_waitcnt vmcnt(8)
	ds_write_b128 v40, v[30:33] offset:4704
	v_mad_u32_u24 v37, v110, s83, v34
	v_mov_b32_e32 v34, 0xab0
	v_mad_u32_u24 v38, v110, s83, v34
	v_lshl_add_u64 v[34:35], s[0:1], 0, v[90:91]
	s_movk_i32 s10, 0x1000
	v_add_co_u32_e32 v92, vcc, s10, v34
	v_mad_u32_u24 v36, v110, s83, s83
	s_nop 0
	v_addc_co_u32_e32 v93, vcc, 0, v35, vcc
	v_add_co_u32_e32 v94, vcc, s10, v94
	global_load_dwordx4 v[20:23], v0, s[6:7]
	global_load_dwordx4 v[78:81], v0, s[6:7] offset:1024
	global_load_dwordx4 v[28:31], v90, s[0:1]
	global_load_dwordx4 v[74:77], v90, s[0:1] offset:1024
	global_load_dwordx4 v[82:85], v0, s[6:7] offset:2048
	global_load_dwordx4 v[66:69], v0, s[6:7] offset:3072
	global_load_dwordx4 v[86:89], v[92:93], off
	global_load_dwordx4 v[70:73], v[92:93], off offset:1024
	s_waitcnt vmcnt(15)
	ds_write_b128 v40, v[200:203] offset:9216
	s_waitcnt vmcnt(14)
	ds_write_b128 v39, v[206:209] offset:9216
	s_waitcnt vmcnt(13)
	ds_write_b128 v40, v[210:213] offset:9248
	s_waitcnt vmcnt(12)
	ds_write_b128 v39, v[232:235] offset:9248
	s_waitcnt vmcnt(11)
	ds_write_b128 v40, v[236:239] offset:9280
	s_waitcnt vmcnt(10)
	ds_write_b128 v40, v[240:243] offset:13888
	s_waitcnt vmcnt(9)
	ds_write_b128 v40, v[244:247] offset:9312
	s_waitcnt vmcnt(8)
; __device__ __forceinline__ float bf2f(bf16_t b) { return __uint_as_float(((unsigned)b) << 16); }
; __device__ __forceinline__ void ph_rwkv_out(const Params& p, int l, LAS unsigned char* lds, const int wvid) {
;     ...
;             for (int x = 0; x < 2; ++x) { ga[ks][x] = *(const bf16x8*)(GTg + TM(32 * x + l31, 16 * ks + 8 * hi)); sb[ks][x] = __builtin_bit_cast(bf16x8, SH[(x * 4 + ks) * 64 + lane]); }
; #pragma unroll
;         for (int rb = 0; rb < 2; ++rb)
; #pragma unroll
;             for (int cb = 0; cb < 2; ++cb)
; #pragma unroll
;                 for (int r = 0; r < 16; ++r) yl[rb][cb][r] = (unsigned short)R2_RD16(Y, 32 * rb + (r & 3) + 8 * (r >> 2) + 4 * hi, 32 * cb + l31);
;         M64 Yt;
; #pragma unroll
;         for (int rb = 0; rb < 2; ++rb)
; #pragma unroll
;             for (int cb = 0; cb < 2; ++cb)
; #pragma unroll
;                 for (int r = 0; r < 16; ++r) Yt[rb][cb][r] = bf2f(yl[rb][cb][r]);
; #pragma unroll
;         for (int ks = 0; ks < 4; ++ks)
; #pragma unroll
;             for (int rb = 0; rb < 2; ++rb)
; #pragma unroll
;                 for (int cb = 0; cb < 2; ++cb) Yt[rb][cb] = __builtin_amdgcn_mfma_f32_32x32x16_bf16(ga[ks][rb], sb[ks][cb], Yt[rb][cb], 0, 0, 0);
	ds_write_b128 v40, v[196:199] offset:13920
	v_lshlrev_b32_e32 v0, 1, v100
	v_add_u32_e32 v111, s34, v0
	s_movk_i32 s6, 0x240
	v_mad_u32_u24 v2, v103, s6, v111
	v_mad_u32_u24 v148, v98, s83, v111
	v_mad_u32_u24 v3, v110, s83, v111
	v_add_u32_e32 v114, v111, v36
	v_add_u32_e32 v113, v111, v37
	v_add_u32_e32 v112, v111, v38
	ds_read_u16 v4, v148 offset:9216
	ds_read_u16 v5, v148 offset:9360
	ds_read_u16 v6, v148 offset:9504
	ds_read_u16 v7, v148 offset:10224
	ds_read_u16 v8, v148 offset:10288
	ds_read_u16 v9, v148 offset:9568
	ds_read_u16 v10, v148 offset:9424
	ds_read_u16 v11, v148 offset:9280
	ds_read_u16 v12, v148 offset:10368
	ds_read_u16 v13, v148 offset:10512
	ds_read_u16 v14, v148 offset:10656
	ds_read_u16 v15, v148 offset:11376
	ds_read_u16 v16, v148 offset:11440
	ds_read_u16 v17, v148 offset:10720
	ds_read_u16 v18, v148 offset:10576
	ds_read_u16 v19, v148 offset:10432
	ds_read_u16 v24, v148 offset:11520
	ds_read_u16 v25, v148 offset:11664
	ds_read_u16 v26, v148 offset:11808
	ds_read_u16 v27, v148 offset:12528
	ds_read_u16 v32, v148 offset:12592
	ds_read_u16 v33, v148 offset:11872
	ds_read_u16 v60, v148 offset:11728
	ds_read_u16 v58, v148 offset:11584
	ds_read_u16 v46, v148 offset:12672
	ds_read_u16 v48, v148 offset:12816
	ds_read_u16 v49, v148 offset:12960
	ds_read_u16 v64, v148 offset:13024
	ds_read_u16 v102, v3 offset:9216
	ds_read_u16 v104, v3 offset:9280
	ds_read_u16 v3, v148 offset:12880
	ds_read_u16 v62, v148 offset:12736
	ds_read_u16 v106, v114 offset:9216
	ds_read_u16 v107, v114 offset:9360
	ds_read_u16 v108, v114 offset:9504
	ds_read_u16 v109, v114 offset:10224
	ds_read_u16 v115, v114 offset:10288
	ds_read_u16 v116, v114 offset:9568
	ds_read_u16 v117, v114 offset:9424
	ds_read_u16 v118, v114 offset:9280
	ds_read_u16 v119, v114 offset:10368
	ds_read_u16 v120, v113 offset:9216
	ds_read_u16 v121, v113 offset:9360
	ds_read_u16 v122, v113 offset:10080
	ds_read_u16 v123, v113 offset:10144
	ds_read_u16 v124, v113 offset:9424
	ds_read_u16 v125, v113 offset:9280
	ds_read_u16 v126, v114 offset:10432
	ds_read_u16 v127, v113 offset:10224
	ds_read_u16 v128, v113 offset:10368
	ds_read_u16 v129, v112 offset:9216
	ds_read_u16 v130, v112 offset:9936
	ds_read_u16 v131, v112 offset:10000
	ds_read_u16 v132, v112 offset:9280
	ds_read_u16 v133, v113 offset:10432
	ds_read_u16 v134, v113 offset:10288
	ds_read_u16 v135, v112 offset:10080
	ds_read_u16 v136, v112 offset:10224
	ds_read_u16 v137, v112 offset:10368
	ds_read_u16 v138, v112 offset:10432
	ds_read_u16 v139, v112 offset:10288
	ds_read_u16 v140, v112 offset:10144
	ds_read_u16 v34, v2 offset:9216
	ds_read_u16 v2, v2 offset:9280
	ds_read_u16 v141, v148
	ds_read_u16 v105, v148 offset:64
	ds_read_u16 v101, v148 offset:144
	ds_read_u16 v99, v148 offset:208
	ds_read_u16 v97, v148 offset:288
	ds_read_u16 v91, v148 offset:352
	s_waitcnt lgkmcnt(14)
	v_lshlrev_b32_e32 v35, 16, v4
	s_waitcnt lgkmcnt(7)
	v_lshlrev_b32_e32 v34, 16, v34
	v_lshlrev_b32_e32 v37, 16, v6
	v_lshlrev_b32_e32 v36, 16, v5
	v_lshlrev_b32_e32 v39, 16, v12
	v_lshlrev_b32_e32 v38, 16, v7
	v_lshlrev_b32_e32 v41, 16, v14
	v_lshlrev_b32_e32 v40, 16, v13
	v_lshlrev_b32_e32 v43, 16, v24
	v_lshlrev_b32_e32 v42, 16, v15
	v_lshlrev_b32_e32 v45, 16, v26
	v_lshlrev_b32_e32 v44, 16, v25
	v_lshlrev_b32_e32 v47, 16, v46
	v_lshlrev_b32_e32 v46, 16, v27
	v_lshlrev_b32_e32 v49, 16, v49
	v_lshlrev_b32_e32 v48, 16, v48
	v_lshlrev_b32_e32 v51, 16, v11
	s_waitcnt lgkmcnt(6)
	v_lshlrev_b32_e32 v50, 16, v2
	v_lshlrev_b32_e32 v53, 16, v9
	v_lshlrev_b32_e32 v52, 16, v10
	v_lshlrev_b32_e32 v54, 16, v8
	v_lshlrev_b32_e32 v57, 16, v17
	v_lshlrev_b32_e32 v59, 16, v58
	v_lshlrev_b32_e32 v58, 16, v16
	v_lshlrev_b32_e32 v65, 16, v64
	v_lshlrev_b32_e32 v64, 16, v3
	v_lshlrev_b32_e32 v3, 16, v106
	v_lshlrev_b32_e32 v2, 16, v102
	v_lshlrev_b32_e32 v5, 16, v108
	v_lshlrev_b32_e32 v4, 16, v107
	v_lshlrev_b32_e32 v7, 16, v119
	v_lshlrev_b32_e32 v6, 16, v109
	v_lshlrev_b32_e32 v9, 16, v121
	v_lshlrev_b32_e32 v8, 16, v120
	v_lshlrev_b32_e32 v11, 16, v127
	v_lshlrev_b32_e32 v10, 16, v122
	v_lshlrev_b32_e32 v13, 16, v129
	v_lshlrev_b32_e32 v12, 16, v128
	v_lshlrev_b32_e32 v15, 16, v135
	v_lshlrev_b32_e32 v14, 16, v130
	v_lshlrev_b32_e32 v17, 16, v137
	v_lshlrev_b32_e32 v16, 16, v136
	v_lshlrev_b32_e32 v55, 16, v19
	v_lshlrev_b32_e32 v56, 16, v18
	v_lshlrev_b32_e32 v61, 16, v33
	v_lshlrev_b32_e32 v60, 16, v60
	v_lshlrev_b32_e32 v63, 16, v62
	v_lshlrev_b32_e32 v62, 16, v32
	v_lshlrev_b32_e32 v19, 16, v118
	v_lshlrev_b32_e32 v18, 16, v104
	v_lshlrev_b32_e32 v25, 16, v124
	v_lshlrev_b32_e32 v24, 16, v125
	s_waitcnt vmcnt(5)
	v_mfma_f32_32x32x16_bf16 v[34:49], v[20:23], v[28:31], v[34:49]
	v_lshlrev_b32_e32 v27, 16, v134
	v_lshlrev_b32_e32 v26, 16, v123
	v_lshlrev_b32_e32 v33, 16, v138
	v_lshlrev_b32_e32 v32, 16, v139
	v_addc_co_u32_e32 v95, vcc, 0, v95, vcc
	v_cmp_gt_u32_e32 vcc, 32, v222
	v_mfma_f32_32x32x16_bf16 v[2:17], v[78:81], v[28:31], v[2:17]
	v_lshlrev_b32_e32 v29, 16, v132
	v_lshlrev_b32_e32 v28, 16, v133
	v_lshlrev_b32_e32 v31, 16, v140
	v_lshlrev_b32_e32 v30, 16, v131
	s_waitcnt vmcnt(1)
	v_mfma_f32_32x32x16_bf16 v[50:65], v[20:23], v[86:89], v[50:65]
	v_lshlrev_b32_e32 v21, 16, v116
	v_lshlrev_b32_e32 v20, 16, v117
	v_lshlrev_b32_e32 v23, 16, v126
	v_lshlrev_b32_e32 v22, 16, v115
	s_nop 1
	v_mfma_f32_32x32x16_bf16 v[18:33], v[78:81], v[86:89], v[18:33]
	v_mfma_f32_32x32x16_bf16 v[34:49], v[82:85], v[74:77], v[34:49]
	v_mfma_f32_32x32x16_bf16 v[2:17], v[66:69], v[74:77], v[2:17]
	global_load_dwordx4 v[74:77], v[94:95], off
	s_waitcnt vmcnt(1)
; __device__ __forceinline__ void ph_rwkv_out(const Params& p, int l, LAS unsigned char* lds, const int wvid) {
;     ...
;         for (int ks = 0; ks < 4; ++ks)
; #pragma unroll
;             for (int rb = 0; rb < 2; ++rb)
; #pragma unroll
;                 for (int cb = 0; cb < 2; ++cb) Yt[rb][cb] = __builtin_amdgcn_mfma_f32_32x32x16_bf16(ga[ks][rb], sb[ks][cb], Yt[rb][cb], 0, 0, 0);
;         const float lg0 = p.in[I_LNXG][l * 256 + h * 64 + l31], lg1 = p.in[I_LNXG][l * 256 + h * 64 + 32 + l31], lb0 = p.in[I_LNXB][l * 256 + h * 64 + l31], lb1 = p.in[I_LNXB][l * 256 + h * 64 + 32 + l31];
; #pragma unroll
;         for (int rb = 0; rb < 2; ++rb) {
;             unsigned short v0[16], v1[16], g0[16], g1[16]; float bcv[16];
; #pragma unroll
;             for (int r = 0; r < 16; ++r) { const int t = 32 * rb + (r & 3) + 8 * (r >> 2) + 4 * hi; const int tg = min(t0 + t, LT - 1); const size_t row = (size_t)b * LT + tg;
;                 v0[r] = (unsigned short)R2_RD16(X, t, l31); v1[r] = (unsigned short)R2_RD16(X, t, 32 + l31); g0[r] = Gg[row * 256 + h * 64 + l31]; g1[r] = Gg[row * 256 + h * 64 + 32 + l31]; bcv[r] = BCg[row * 4 + h]; }
	v_mfma_f32_32x32x16_bf16 v[50:65], v[82:85], v[70:73], v[50:65]
	v_mfma_f32_32x32x16_bf16 v[18:33], v[66:69], v[70:73], v[18:33]
	global_load_dwordx4 v[70:73], v90, s[0:1] offset:2048
	global_load_dwordx4 v[78:81], v[94:95], off offset:1024
	global_load_dwordx4 v[82:85], v90, s[0:1] offset:3072
	global_load_dwordx4 v[86:89], v[92:93], off offset:2048
	global_load_dwordx4 v[66:69], v[92:93], off offset:3072
	s_lshl_b32 s0, s9, 7
	s_add_u32 s6, s22, s0
	s_addc_u32 s7, s23, 0
	s_lshl_b32 s1, s9, 2
	s_add_u32 s10, s24, s1
	s_addc_u32 s11, s25, 0
	s_waitcnt vmcnt(4)
	v_mfma_f32_32x32x16_bf16 v[34:49], v[74:77], v[70:73], v[34:49]
	s_waitcnt vmcnt(1)
	v_mfma_f32_32x32x16_bf16 v[50:65], v[74:77], v[86:89], v[50:65]
	global_load_dwordx4 v[74:77], v[94:95], off offset:2048
	v_mfma_f32_32x32x16_bf16 v[2:17], v[78:81], v[70:73], v[2:17]
	global_load_dwordx4 v[70:73], v[94:95], off offset:3072
	v_mfma_f32_32x32x16_bf16 v[18:33], v[78:81], v[86:89], v[18:33]
	v_or_b32_e32 v78, s40, v100
	v_mov_b32_e32 v79, v1
	v_lshl_or_b32 v78, s9, 6, v78
	v_lshlrev_b64 v[78:79], 2, v[78:79]
	v_lshl_add_u64 v[80:81], s[54:55], 0, v[78:79]
	v_lshl_add_u64 v[78:79], s[56:57], 0, v[78:79]
	global_load_dword v109, v[80:81], off
	global_load_dword v107, v[80:81], off offset:128
	global_load_dword v108, v[78:79], off
	global_load_dword v106, v[78:79], off offset:128
	s_waitcnt vmcnt(5)
	v_mfma_f32_32x32x16_bf16 v[34:49], v[74:77], v[82:85], v[34:49]
	s_mul_hi_i32 s9, s8, 0x1010
	v_mfma_f32_32x32x16_bf16 v[50:65], v[74:77], v[66:69], v[50:65]
	v_or_b32_e32 v76, s35, v96
	v_or_b32_e32 v77, s35, v98
	v_or_b32_e32 v102, 3, v76
	v_min_i32_e32 v78, 0x100f, v77
	v_or_b32_e32 v104, 2, v76
	v_min_i32_e32 v86, 0x100f, v102
	v_ashrrev_i32_e32 v79, 31, v78
	s_waitcnt vmcnt(4)
	v_mfma_f32_32x32x16_bf16 v[2:17], v[70:73], v[82:85], v[2:17]
	v_min_i32_e32 v82, 0x100f, v104
	v_ashrrev_i32_e32 v87, 31, v86
	v_lshl_add_u64 v[74:75], s[6:7], 0, v[0:1]
	v_mad_i64_i32 v[78:79], s[6:7], s8, v251, v[78:79]
	v_ashrrev_i32_e32 v83, 31, v82
	v_mad_i64_i32 v[86:87], s[6:7], s8, v251, v[86:87]
	v_lshlrev_b64 v[80:81], 9, v[78:79]
	v_mad_i64_i32 v[82:83], s[6:7], s8, v251, v[82:83]
	v_lshlrev_b64 v[88:89], 9, v[86:87]
	v_lshl_add_u64 v[80:81], v[74:75], 0, v[80:81]
	v_lshlrev_b64 v[84:85], 9, v[82:83]
	v_lshl_add_u64 v[88:89], v[74:75], 0, v[88:89]
	v_or_b32_e32 v96, 10, v76
	v_lshl_add_u64 v[78:79], v[78:79], 4, s[10:11]
	v_lshl_add_u64 v[84:85], v[74:75], 0, v[84:85]
	v_lshl_add_u64 v[82:83], v[82:83], 4, s[10:11]
	global_load_ushort v167, v[80:81], off
	global_load_ushort v165, v[80:81], off offset:64
	global_load_dword v166, v[78:79], off
	v_min_i32_e32 v196, 0x100f, v76
	v_ashrrev_i32_e32 v197, 31, v196
	v_mad_i64_i32 v[196:197], s[6:7], s8, v251, v[196:197]
	v_lshlrev_b64 v[198:199], 9, v[196:197]
	v_lshl_add_u64 v[198:199], v[74:75], 0, v[198:199]
	v_lshl_add_u64 v[196:197], v[196:197], 4, s[10:11]
	global_load_ushort v185, v[198:199], off
	global_load_ushort v186, v[198:199], off offset:64
	global_load_dword v184, v[196:197], off
	global_load_ushort v162, v[84:85], off
	global_load_ushort v160, v[84:85], off offset:64
	global_load_dword v161, v[82:83], off
	global_load_ushort v156, v[88:89], off
	global_load_ushort v155, v[88:89], off offset:64
	v_or_b32_e32 v100, 8, v76
	v_or_b32_e32 v98, 9, v76
	v_min_i32_e32 v88, 0x100f, v96
	v_min_i32_e32 v80, 0x100f, v100
	v_min_i32_e32 v84, 0x100f, v98
	v_ashrrev_i32_e32 v89, 31, v88
	v_ashrrev_i32_e32 v81, 31, v80
	v_ashrrev_i32_e32 v85, 31, v84
	v_mad_i64_i32 v[88:89], s[6:7], s8, v251, v[88:89]
	v_mad_i64_i32 v[80:81], s[6:7], s8, v251, v[80:81]
	v_mad_i64_i32 v[84:85], s[6:7], s8, v251, v[84:85]
	v_lshlrev_b64 v[92:93], 9, v[88:89]
	v_lshl_add_u64 v[78:79], v[86:87], 4, s[10:11]
	v_lshlrev_b64 v[82:83], 9, v[80:81]
	v_lshl_add_u64 v[80:81], v[80:81], 4, s[10:11]
	v_lshlrev_b64 v[86:87], 9, v[84:85]
	v_lshl_add_u64 v[84:85], v[84:85], 4, s[10:11]
	v_lshl_add_u64 v[116:117], v[74:75], 0, v[92:93]
	v_or_b32_e32 v94, 11, v76
	v_or_b32_e32 v92, 16, v76
	v_lshl_add_u64 v[82:83], v[74:75], 0, v[82:83]
	v_lshl_add_u64 v[86:87], v[74:75], 0, v[86:87]
	global_load_dword v159, v[78:79], off
	global_load_ushort v154, v[82:83], off
	global_load_ushort v152, v[82:83], off offset:64
	global_load_dword v153, v[80:81], off
	global_load_ushort v149, v[86:87], off
	global_load_ushort v146, v[86:87], off offset:64
	global_load_dword v147, v[84:85], off
	global_load_ushort v95, v[116:117], off
	v_min_i32_e32 v80, 0x100f, v94
	v_min_i32_e32 v84, 0x100f, v92
	v_ashrrev_i32_e32 v81, 31, v80
	v_ashrrev_i32_e32 v85, 31, v84
	v_mad_i64_i32 v[80:81], s[6:7], s8, v251, v[80:81]
	v_mad_i64_i32 v[84:85], s[6:7], s8, v251, v[84:85]
	v_lshlrev_b64 v[82:83], 9, v[80:81]
	v_lshlrev_b64 v[86:87], 9, v[84:85]
	v_lshl_add_u64 v[78:79], v[88:89], 4, s[10:11]
	v_lshl_add_u64 v[82:83], v[74:75], 0, v[82:83]
	v_lshl_add_u64 v[86:87], v[74:75], 0, v[86:87]
	v_or_b32_e32 v90, 17, v76
	v_or_b32_e32 v88, 18, v76
	v_lshl_add_u64 v[80:81], v[80:81], 4, s[10:11]
	v_lshl_add_u64 v[84:85], v[84:85], 4, s[10:11]
	global_load_ushort v142, v[116:117], off offset:64
	global_load_dword v143, v[78:79], off
	global_load_ushort v139, v[82:83], off
	global_load_ushort v93, v[82:83], off offset:64
	global_load_dword v137, v[80:81], off
	global_load_ushort v135, v[86:87], off
	global_load_ushort v132, v[86:87], off offset:64
	global_load_dword v133, v[84:85], off
	v_min_i32_e32 v78, 0x100f, v90
	v_min_i32_e32 v82, 0x100f, v88
	v_or_b32_e32 v86, 19, v76
	v_ashrrev_i32_e32 v79, 31, v78
	v_ashrrev_i32_e32 v83, 31, v82
	v_min_i32_e32 v116, 0x100f, v86
	v_mad_i64_i32 v[78:79], s[6:7], s8, v251, v[78:79]
; __device__ __forceinline__ float bf2f(bf16_t b) { return __uint_as_float(((unsigned)b) << 16); }
; __device__ __forceinline__ bf16_t f2bf(float f) { unsigned u = __float_as_uint(f); u += 0x7FFFu + ((u >> 16) & 1u); return (bf16_t)(u >> 16); }
; __device__ __forceinline__ float frsq(float x) { return __builtin_amdgcn_rsqf(x); }
; __device__ __forceinline__ float half_sum32(float v) {
;     v = row_sum16(v); v = dpp_add<0x142, 0xA>(v);
;     const float lo = __int_as_float(__builtin_amdgcn_readlane(__float_as_int(v), 31)), hi = __int_as_float(__builtin_amdgcn_readlane(__float_as_int(v), 63));
;     return (__builtin_amdgcn_mbcnt_hi(~0u, __builtin_amdgcn_mbcnt_lo(~0u, 0u)) < 32u) ? lo : hi;
; }
; __device__ __forceinline__ void ph_rwkv_out(const Params& p, int l, LAS unsigned char* lds, const int wvid) {
;     ...
;             for (int r = 0; r < 16; ++r) { const int t = 32 * rb + (r & 3) + 8 * (r >> 2) + 4 * hi; const int tg = min(t0 + t, LT - 1); const size_t row = (size_t)b * LT + tg;
;                 v0[r] = (unsigned short)R2_RD16(X, t, l31); v1[r] = (unsigned short)R2_RD16(X, t, 32 + l31); g0[r] = Gg[row * 256 + h * 64 + l31]; g1[r] = Gg[row * 256 + h * 64 + 32 + l31]; bcv[r] = BCg[row * 4 + h]; }
; #pragma unroll
;             for (int r = 0; r < 16; ++r) { const int t = 32 * rb + (r & 3) + 8 * (r >> 2) + 4 * hi, tg = t0 + t;
;                 const float y0 = Yt[rb][0][r], y1 = Yt[rb][1][r];
;                 const float mean = half_sum32(y0 + y1) * (1.f / 64.f); const float d0 = y0 - mean, d1 = y1 - mean;
;                 const float var = half_sum32(d0 * d0 + d1 * d1) * (1.f / 64.f); const float rs = frsq(var + 64e-5f);
;                 if (tg < LT) { const size_t row = (size_t)b * LT + tg;
;                     const float o0 = (d0 * rs * lg0 + lb0 + bcv[r] * bf2f(v0[r])) * bf2f(g0[r]);
;                     const float o1 = (d1 * rs * lg1 + lb1 + bcv[r] * bf2f(v1[r])) * bf2f(g1[r]);
;                     MIX[row * D + M_C + h * 64 + l31] = f2bf(o0); MIX[row * D + M_C + h * 64 + 32 + l31] = f2bf(o1); } }
	v_mad_i64_i32 v[82:83], s[6:7], s8, v251, v[82:83]
	v_ashrrev_i32_e32 v117, 31, v116
	v_lshlrev_b64 v[80:81], 9, v[78:79]
	v_lshlrev_b64 v[84:85], 9, v[82:83]
	v_mad_i64_i32 v[116:117], s[6:7], s8, v251, v[116:117]
	v_lshl_add_u64 v[80:81], v[74:75], 0, v[80:81]
	v_lshl_add_u64 v[84:85], v[74:75], 0, v[84:85]
	v_lshlrev_b64 v[118:119], 9, v[116:117]
	v_lshl_add_u64 v[78:79], v[78:79], 4, s[10:11]
	v_lshl_add_u64 v[82:83], v[82:83], 4, s[10:11]
	v_lshl_add_u64 v[118:119], v[74:75], 0, v[118:119]
	global_load_ushort v131, v[80:81], off
	global_load_ushort v89, v[80:81], off offset:64
	global_load_dword v130, v[78:79], off
	global_load_ushort v127, v[84:85], off
	global_load_ushort v87, v[84:85], off offset:64
	global_load_dword v126, v[82:83], off
	global_load_ushort v124, v[118:119], off
	s_nop 0
	global_load_ushort v85, v[118:119], off offset:64
	v_or_b32_e32 v84, 24, v76
	v_min_i32_e32 v80, 0x100f, v84
	v_ashrrev_i32_e32 v81, 31, v80
	v_mad_i64_i32 v[80:81], s[6:7], s8, v251, v[80:81]
	v_lshlrev_b64 v[82:83], 9, v[80:81]
	v_lshl_add_u64 v[78:79], v[116:117], 4, s[10:11]
	v_lshl_add_u64 v[116:117], v[74:75], 0, v[82:83]
	v_or_b32_e32 v82, 25, v76
	v_lshl_add_u64 v[118:119], v[80:81], 4, s[10:11]
	v_min_i32_e32 v80, 0x100f, v82
	v_ashrrev_i32_e32 v81, 31, v80
	v_mad_i64_i32 v[80:81], s[6:7], s8, v251, v[80:81]
	v_lshlrev_b64 v[120:121], 9, v[80:81]
	v_lshl_add_u64 v[144:145], v[80:81], 4, s[10:11]
	v_or_b32_e32 v80, 26, v76
	v_lshl_add_u64 v[128:129], v[74:75], 0, v[120:121]
	v_min_i32_e32 v120, 0x100f, v80
	v_ashrrev_i32_e32 v121, 31, v120
	v_mad_i64_i32 v[150:151], s[6:7], s8, v251, v[120:121]
	v_lshlrev_b64 v[120:121], 9, v[150:151]
	v_lshl_add_u64 v[168:169], v[74:75], 0, v[120:121]
	global_load_dword v125, v[78:79], off
	global_load_ushort v123, v[116:117], off
	global_load_ushort v83, v[116:117], off offset:64
	global_load_dword v122, v[118:119], off
	global_load_ushort v121, v[128:129], off
	global_load_ushort v81, v[128:129], off offset:64
	global_load_dword v120, v[144:145], off
	global_load_ushort v79, v[168:169], off
	v_or_b32_e32 v78, 27, v76
	v_min_i32_e32 v118, 0x100f, v78
	v_ashrrev_i32_e32 v119, 31, v118
	v_mad_i64_i32 v[118:119], s[6:7], s8, v251, v[118:119]
	v_lshl_add_u64 v[116:117], v[150:151], 4, s[10:11]
	v_lshlrev_b64 v[128:129], 9, v[118:119]
	v_lshl_add_u64 v[128:129], v[74:75], 0, v[128:129]
	v_lshl_add_u64 v[144:145], v[118:119], 4, s[10:11]
	global_load_ushort v118, v[168:169], off offset:64
	global_load_dword v119, v[116:117], off
	s_nop 0
	global_load_ushort v117, v[128:129], off
	global_load_ushort v115, v[128:129], off offset:64
	global_load_dword v116, v[144:145], off
	v_mfma_f32_32x32x16_bf16 v[18:33], v[70:73], v[66:69], v[18:33]
	ds_read_u16 v169, v148 offset:1008
	ds_read_u16 v168, v148 offset:1072
	ds_read_u16 v164, v148 offset:1152
	ds_read_u16 v163, v148 offset:1216
	ds_read_u16 v158, v148 offset:1296
	ds_read_u16 v157, v148 offset:1360
	ds_read_u16 v151, v148 offset:1440
	ds_read_u16 v150, v148 offset:1504
	ds_read_u16 v145, v148 offset:2160
	ds_read_u16 v144, v148 offset:2224
	ds_read_u16 v140, v148 offset:2304
	ds_read_u16 v138, v148 offset:2368
	ds_read_u16 v136, v148 offset:2448
	ds_read_u16 v134, v148 offset:2512
	ds_read_u16 v129, v148 offset:2592
	ds_read_u16 v128, v148 offset:2656
	ds_read_u16 v73, v148 offset:3312
	ds_read_u16 v72, v148 offset:3376
	ds_read_u16 v71, v148 offset:3456
	ds_read_u16 v70, v148 offset:3520
	ds_read_u16 v69, v148 offset:3600
	ds_read_u16 v68, v148 offset:3664
	ds_read_u16 v67, v148 offset:3744
	ds_read_u16 v66, v148 offset:3808
	v_add_f32_e32 v77, v34, v50
	v_mov_b32_e32 v148, v1
	s_add_u32 s6, s18, s0
	v_add_f32_dpp v77, v77, v77 quad_perm:[1,0,3,2] row_mask:0xf bank_mask:0xf bound_ctrl:1
	s_mulk_i32 s8, 0x1010
	s_addc_u32 s7, s19, 0
	v_add_f32_dpp v77, v77, v77 quad_perm:[2,3,0,1] row_mask:0xf bank_mask:0xf bound_ctrl:1
	s_nop 1
	v_add_f32_dpp v77, v77, v77 row_half_mirror row_mask:0xf bank_mask:0xf bound_ctrl:1
	s_nop 1
	v_add_f32_dpp v77, v77, v77 row_mirror row_mask:0xf bank_mask:0xf bound_ctrl:1
	s_nop 1
	v_mov_b32_dpp v148, v77 row_bcast:15 row_mask:0xa bank_mask:0xf
	v_add_f32_e32 v77, v77, v148
	s_nop 0
	v_readlane_b32 s0, v77, 31
	v_readlane_b32 s1, v77, 63
	s_nop 0
	v_mov_b32_e32 v148, s0
	v_mov_b32_e32 v77, s1
	v_cndmask_b32_e32 v77, v77, v148, vcc
	v_fmamk_f32 v148, v77, 0xbc800000, v34
	v_fmamk_f32 v34, v77, 0xbc800000, v50
	v_mul_f32_e32 v50, v34, v34
	v_fmac_f32_e32 v50, v148, v148
	v_mov_b32_e32 v77, v1
	v_cmp_gt_i32_e64 s[0:1], s33, v76
	v_add_f32_dpp v50, v50, v50 quad_perm:[1,0,3,2] row_mask:0xf bank_mask:0xf bound_ctrl:1
	s_nop 1
	v_add_f32_dpp v50, v50, v50 quad_perm:[2,3,0,1] row_mask:0xf bank_mask:0xf bound_ctrl:1
	s_nop 1
	v_add_f32_dpp v50, v50, v50 row_half_mirror row_mask:0xf bank_mask:0xf bound_ctrl:1
	s_nop 1
	v_add_f32_dpp v50, v50, v50 row_mirror row_mask:0xf bank_mask:0xf bound_ctrl:1
	s_nop 1
	v_mov_b32_dpp v77, v50 row_bcast:15 row_mask:0xa bank_mask:0xf
	v_add_f32_e32 v50, v50, v77
	s_nop 0
	v_readlane_b32 s36, v50, 31
	v_readlane_b32 s37, v50, 63
	s_and_saveexec_b64 s[16:17], s[0:1]
	s_cbranch_execz .LBB0_858
	v_ashrrev_i32_e32 v77, 31, v76
	v_lshl_add_u64 v[170:171], s[8:9], 0, v[76:77]
	v_lshl_add_u64 v[172:173], v[170:171], 4, s[10:11]
	s_nop 0
	v_mul_u32_u24_e32 v50, 0x240, v103
	v_mov_b32_e32 v103, s37
	v_mov_b32_e32 v174, s36
	v_cndmask_b32_e32 v103, v103, v174, vcc
	v_add_u32_e32 v50, v111, v50
	v_fmamk_f32 v103, v103, 0x3c800000, v249
	v_rsq_f32_e32 v103, v103
	ds_read_u16 v174, v50
	ds_read_u16 v50, v50 offset:64
	v_lshlrev_b64 v[172:173], 9, v[170:171]
	v_mul_f32_e32 v148, v148, v103
	v_lshl_add_u64 v[172:173], v[74:75], 0, v[172:173]
	s_waitcnt vmcnt(47)
	v_fma_f32 v148, v109, v148, v108
	s_waitcnt lgkmcnt(1)
	v_lshlrev_b32_e32 v174, 16, v174
	v_mul_f32_e32 v34, v34, v103
	s_waitcnt vmcnt(46)
	v_fma_f32 v34, v107, v34, v106
	s_waitcnt lgkmcnt(0)
	v_lshlrev_b32_e32 v50, 16, v50
	v_lshlrev_b64 v[170:171], 11, v[170:171]
	v_lshl_add_u64 v[170:171], s[6:7], 0, v[170:171]
	v_lshl_add_u64 v[170:171], v[170:171], 0, v[0:1]
	s_waitcnt vmcnt(0)
	v_fmac_f32_e32 v148, v184, v174
	v_mov_b32_e32 v174, v185
	v_fmac_f32_e32 v34, v184, v50
	v_mov_b32_e32 v50, v186
	s_nop 0
	v_lshlrev_b32_e32 v174, 16, v174
	v_mul_f32_e32 v148, v148, v174
	s_nop 0
	v_lshlrev_b32_e32 v50, 16, v50
	v_mul_f32_e32 v34, v34, v50
	v_bfe_u32 v50, v148, 16, 1
	v_add3_u32 v50, v148, v50, s79
	global_store_short_d16_hi v[170:171], v50, off offset:1024
	v_bfe_u32 v50, v34, 16, 1
	v_add3_u32 v34, v34, v50, s79
	global_store_short_d16_hi v[170:171], v34, off offset:1088
